# cache-policy lever: nt hint also on the residual-row (x) loads of the combine+norm1 pass, which are overwritten in the same pass, so that they do not displace the MoE output rows still to be gathered
# baseline (speedup 1.0000x reference)
; __device__ __forceinline__ float* xrow_ptr(float* xl, float* xc, int b, int t) { return (t < SEQ) ? xl + ((size_t)(b * SEQ + t)) * DM : xc + ((size_t)(b * CTXL + (t - SEQ))) * DM; }
; #define xl OUTP(launder(kargs))
; __device__ __forceinline__ void norm1_phase(Frame& F, KArgs a, int L) {
;     ...
;             int r = r0 + k * F.NGW; ok[k] = r < NR; if (!ok[k]) r = r0;
;             const int b = r / TPS, t = r - b * TPS; const bool isctx = t >= SEQ; ss[k] = isctx ? 8 : b; rw[k] = r;
;             if (L == 4 && isctx) ok[k] = false;
;             xr[k] = xrow_ptr(xl, xc, b, t);
;             const float* src = (L == 0) ? (isctx ? cin + ((size_t)(b * CTXL + t - SEQ)) * DM : xin + ((size_t)(b * SEQ + t)) * DM) : xr[k];
; #pragma unroll
;             for (int j = 0; j < 4; ++j) v[k][j] = *(const f32x4*)(src + 256 * j + 4 * lane);
;             sl[k] = -1; af[k] = 0.f;
;             if (L > 0 && lane < 16) { sl[k] = SLOT[(size_t)r * 16 + lane]; af[k] = AFF[(size_t)r * 16 + lane]; }
.LBB0_181:
	global_load_dwordx4 v[30:33], v194, s[10:11] nt
	global_load_dwordx4 v[26:29], v194, s[10:11] offset:1024 nt
	global_load_dwordx4 v[22:25], v194, s[10:11] offset:2048 nt
	global_load_dwordx4 v[18:21], v194, s[10:11] offset:3072 nt
	v_mov_b32_e32 v101, 0
	v_mov_b32_e32 v100, -1
	s_and_saveexec_b64 s[10:11], s[34:35]
	s_cbranch_execz .LBB0_183
	s_ashr_i32 s7, s6, 31
	s_lshl_b64 s[24:25], s[6:7], 6
	v_lshl_or_b32 v2, v38, 2, s24
	v_mov_b32_e32 v3, s25
	v_lshl_add_u64 v[4:5], s[22:23], 0, v[2:3]
	v_lshl_add_u64 v[2:3], s[20:21], 0, v[2:3]
	global_load_dword v100, v[4:5], off
	global_load_dword v101, v[2:3], off

; __device__ __forceinline__ float* xrow_ptr(float* xl, float* xc, int b, int t) { return (t < SEQ) ? xl + ((size_t)(b * SEQ + t)) * DM : xc + ((size_t)(b * CTXL + (t - SEQ))) * DM; }
; #define xl OUTP(launder(kargs))
; __device__ __forceinline__ void norm1_phase(Frame& F, KArgs a, int L) {
;     ...
;             int r = r0 + k * F.NGW; ok[k] = r < NR; if (!ok[k]) r = r0;
;             const int b = r / TPS, t = r - b * TPS; const bool isctx = t >= SEQ; ss[k] = isctx ? 8 : b; rw[k] = r;
;             if (L == 4 && isctx) ok[k] = false;
;             xr[k] = xrow_ptr(xl, xc, b, t);
;             const float* src = (L == 0) ? (isctx ? cin + ((size_t)(b * CTXL + t - SEQ)) * DM : xin + ((size_t)(b * SEQ + t)) * DM) : xr[k];
; #pragma unroll
;             for (int j = 0; j < 4; ++j) v[k][j] = *(const f32x4*)(src + 256 * j + 4 * lane);
;             sl[k] = -1; af[k] = 0.f;
;             if (L > 0 && lane < 16) { sl[k] = SLOT[(size_t)r * 16 + lane]; af[k] = AFF[(size_t)r * 16 + lane]; }
.LBB0_192:
	global_load_dwordx4 v[14:17], v194, s[4:5] nt
	global_load_dwordx4 v[10:13], v194, s[4:5] offset:1024 nt
	global_load_dwordx4 v[6:9], v194, s[4:5] offset:2048 nt
	global_load_dwordx4 v[2:5], v194, s[4:5] offset:3072 nt
	v_mov_b32_e32 v99, 0
	v_mov_b32_e32 v98, -1
	s_and_saveexec_b64 s[4:5], s[34:35]
	s_cbranch_execz .LBB0_194
	s_ashr_i32 s11, s10, 31
	s_lshl_b64 s[24:25], s[10:11], 6
	v_lshl_or_b32 v34, v38, 2, s24
	v_mov_b32_e32 v35, s25
	v_lshl_add_u64 v[36:37], s[22:23], 0, v[34:35]
	v_lshl_add_u64 v[34:35], s[20:21], 0, v[34:35]
	global_load_dword v98, v[36:37], off
	global_load_dword v99, v[34:35], off
